# post-norm-1 router partial-sum reduction rewritten as transposing permlane16/32 swap reduction (same add tree), both layers
# speedup vs baseline: 1.0269x; 1.0170x over previous
; #define LAS __attribute__((address_space(3)))
; __device__ __forceinline__ void ph_post1(Ctx& C, int l, int nrows, bool dry = false) {
;     ...
;             const int e4 = C.lane & 7, cg = C.lane >> 3, cbase = 256 * C.wave + 32 * cg;
;             f32x2 acc[8][2];
; #pragma unroll
;             for (int r = 0; r < 8; ++r) { acc[r][0] = (f32x2){0.f, 0.f}; acc[r][1] = (f32x2){0.f, 0.f}; }
;             const float* wr = INP(I_WR) + (size_t)cbase * NE + 4 * e4;
; #pragma unroll 2
;             for (int cq = 0; cq < 32; cq += 4) {
;                 f32x4 w4[4];
; #pragma unroll
;                 for (int k = 0; k < 4; ++k) w4[k] = *(const f32x4*)(wr + (size_t)(cq + k) * NE);
; #pragma unroll
;                 for (int r = 0; r < 8; ++r) { const f32x4 hv = *(const LAS f32x4*)(H2 + r * DM + cbase + cq);
; #pragma unroll
;                     for (int k = 0; k < 4; ++k) { const f32x2 hh = {hv[k], hv[k]}; acc[r][0] += hh * (f32x2){w4[k][0], w4[k][1]}; acc[r][1] += hh * (f32x2){w4[k][2], w4[k][3]}; } } }
.LBB0_1218:
	global_load_dwordx4 v[22:25], v[74:75], off offset:-896
	global_load_dwordx4 v[14:17], v[74:75], off offset:-768
	global_load_dwordx4 v[10:13], v[74:75], off offset:-640
	global_load_dwordx4 v[6:9], v[74:75], off offset:-512
	ds_read_b128 v[18:21], v102
	ds_read_b128 v[2:5], v102 offset:16
	global_load_dwordx4 v[104:107], v[74:75], off offset:-384
	global_load_dwordx4 v[34:37], v[74:75], off offset:-256
	global_load_dwordx4 v[30:33], v[74:75], off offset:-128
	global_load_dwordx4 v[26:29], v[74:75], off
	ds_read_b128 v[108:111], v102 offset:8192
	ds_read_b128 v[112:115], v102 offset:8208
	ds_read_b128 v[116:119], v102 offset:16384
	ds_read_b128 v[120:123], v102 offset:16400
	ds_read_b128 v[124:127], v102 offset:24576
	ds_read_b128 v[128:131], v102 offset:24592
	ds_read_b128 v[132:135], v102 offset:32768
	ds_read_b128 v[136:139], v102 offset:32784
	ds_read_b128 v[140:143], v102 offset:40960
	ds_read_b128 v[144:147], v102 offset:40976
	ds_read_b128 v[148:151], v102 offset:49152
	ds_read_b128 v[152:155], v102 offset:49168
	ds_read_b128 v[156:159], v102 offset:57344
	ds_read_b128 v[160:163], v102 offset:57360
	s_waitcnt lgkmcnt(13)
	v_mov_b32_e32 v166, v111
	v_mov_b32_e32 v164, v21
	s_waitcnt lgkmcnt(11)
	v_mov_b32_e32 v168, v119
	s_waitcnt lgkmcnt(9)
	v_mov_b32_e32 v170, v127
	s_waitcnt lgkmcnt(7)
	v_mov_b32_e32 v172, v135
	s_waitcnt lgkmcnt(5)
	v_mov_b32_e32 v174, v143
	s_waitcnt lgkmcnt(3)
	v_mov_b32_e32 v176, v151
	s_waitcnt lgkmcnt(1)
	v_mov_b32_e32 v178, v159
	s_add_i32 s8, s8, 8
	v_mov_b32_e32 v180, v5
	v_mov_b32_e32 v182, v115
	v_mov_b32_e32 v184, v123
	v_mov_b32_e32 v186, v131
	v_mov_b32_e32 v188, v139
	v_mov_b32_e32 v190, v147
	v_mov_b32_e32 v192, v155
	s_waitcnt lgkmcnt(0)
	v_mov_b32_e32 v194, v163
	v_lshl_add_u64 v[74:75], v[74:75], 0, s[36:37]
	v_add_u32_e32 v102, 32, v102
	s_cmp_gt_u32 s8, 27
	s_waitcnt vmcnt(7)
	v_pk_fma_f32 v[84:85], v[22:23], v[18:19], v[84:85] op_sel_hi:[1,0,1]
	v_pk_fma_f32 v[82:83], v[24:25], v[18:19], v[82:83] op_sel_hi:[1,0,1]
	v_pk_fma_f32 v[80:81], v[22:23], v[108:109], v[80:81] op_sel_hi:[1,0,1]
	v_pk_fma_f32 v[78:79], v[24:25], v[108:109], v[78:79] op_sel_hi:[1,0,1]
	v_pk_fma_f32 v[76:77], v[22:23], v[116:117], v[76:77] op_sel_hi:[1,0,1]
	v_pk_fma_f32 v[72:73], v[24:25], v[116:117], v[72:73] op_sel_hi:[1,0,1]
	v_pk_fma_f32 v[70:71], v[22:23], v[124:125], v[70:71] op_sel_hi:[1,0,1]
	v_pk_fma_f32 v[52:53], v[24:25], v[124:125], v[52:53] op_sel_hi:[1,0,1]
	v_pk_fma_f32 v[50:51], v[22:23], v[132:133], v[50:51] op_sel_hi:[1,0,1]
	v_pk_fma_f32 v[48:49], v[24:25], v[132:133], v[48:49] op_sel_hi:[1,0,1]
	v_pk_fma_f32 v[46:47], v[22:23], v[140:141], v[46:47] op_sel_hi:[1,0,1]
	v_pk_fma_f32 v[44:45], v[24:25], v[140:141], v[44:45] op_sel_hi:[1,0,1]
	v_pk_fma_f32 v[42:43], v[22:23], v[148:149], v[42:43] op_sel_hi:[1,0,1]
	v_pk_fma_f32 v[40:41], v[24:25], v[148:149], v[40:41] op_sel_hi:[1,0,1]
	v_pk_fma_f32 v[22:23], v[22:23], v[156:157], v[38:39] op_sel_hi:[1,0,1]
	v_pk_fma_f32 v[24:25], v[24:25], v[156:157], v[68:69] op_sel_hi:[1,0,1]
	s_waitcnt vmcnt(6)
	v_pk_fma_f32 v[38:39], v[14:15], v[18:19], v[84:85] op_sel:[0,1,0]
	v_pk_fma_f32 v[18:19], v[16:17], v[18:19], v[82:83] op_sel:[0,1,0]
	v_pk_fma_f32 v[68:69], v[14:15], v[108:109], v[80:81] op_sel:[0,1,0]
	v_pk_fma_f32 v[78:79], v[16:17], v[108:109], v[78:79] op_sel:[0,1,0]
	v_pk_fma_f32 v[76:77], v[14:15], v[116:117], v[76:77] op_sel:[0,1,0]
	v_pk_fma_f32 v[72:73], v[16:17], v[116:117], v[72:73] op_sel:[0,1,0]
	v_pk_fma_f32 v[70:71], v[14:15], v[124:125], v[70:71] op_sel:[0,1,0]
	v_pk_fma_f32 v[52:53], v[16:17], v[124:125], v[52:53] op_sel:[0,1,0]
	v_pk_fma_f32 v[50:51], v[14:15], v[132:133], v[50:51] op_sel:[0,1,0]
	v_pk_fma_f32 v[48:49], v[16:17], v[132:133], v[48:49] op_sel:[0,1,0]
	v_pk_fma_f32 v[46:47], v[14:15], v[140:141], v[46:47] op_sel:[0,1,0]
	v_pk_fma_f32 v[44:45], v[16:17], v[140:141], v[44:45] op_sel:[0,1,0]
	v_pk_fma_f32 v[42:43], v[14:15], v[148:149], v[42:43] op_sel:[0,1,0]
	v_pk_fma_f32 v[40:41], v[16:17], v[148:149], v[40:41] op_sel:[0,1,0]
	v_pk_fma_f32 v[14:15], v[14:15], v[156:157], v[22:23] op_sel:[0,1,0]
	v_pk_fma_f32 v[16:17], v[16:17], v[156:157], v[24:25] op_sel:[0,1,0]
	s_waitcnt vmcnt(5)
	v_pk_fma_f32 v[22:23], v[10:11], v[20:21], v[38:39] op_sel_hi:[1,0,1]
	v_pk_fma_f32 v[18:19], v[12:13], v[20:21], v[18:19] op_sel_hi:[1,0,1]
	v_pk_fma_f32 v[20:21], v[10:11], v[110:111], v[68:69] op_sel_hi:[1,0,1]
	v_pk_fma_f32 v[24:25], v[12:13], v[110:111], v[78:79] op_sel_hi:[1,0,1]
	v_pk_fma_f32 v[38:39], v[10:11], v[118:119], v[76:77] op_sel_hi:[1,0,1]
	v_pk_fma_f32 v[68:69], v[12:13], v[118:119], v[72:73] op_sel_hi:[1,0,1]
	v_pk_fma_f32 v[70:71], v[10:11], v[126:127], v[70:71] op_sel_hi:[1,0,1]
	v_pk_fma_f32 v[52:53], v[12:13], v[126:127], v[52:53] op_sel_hi:[1,0,1]
	v_pk_fma_f32 v[50:51], v[10:11], v[134:135], v[50:51] op_sel_hi:[1,0,1]
	v_pk_fma_f32 v[48:49], v[12:13], v[134:135], v[48:49] op_sel_hi:[1,0,1]
	v_pk_fma_f32 v[46:47], v[10:11], v[142:143], v[46:47] op_sel_hi:[1,0,1]
	v_pk_fma_f32 v[44:45], v[12:13], v[142:143], v[44:45] op_sel_hi:[1,0,1]
	v_pk_fma_f32 v[42:43], v[10:11], v[150:151], v[42:43] op_sel_hi:[1,0,1]
	v_pk_fma_f32 v[40:41], v[12:13], v[150:151], v[40:41] op_sel_hi:[1,0,1]
	v_pk_fma_f32 v[10:11], v[10:11], v[158:159], v[14:15] op_sel_hi:[1,0,1]
	v_pk_fma_f32 v[12:13], v[12:13], v[158:159], v[16:17] op_sel_hi:[1,0,1]
	s_waitcnt vmcnt(4)
; #define LAS __attribute__((address_space(3)))
; __device__ __forceinline__ void ph_post1(Ctx& C, int l, int nrows, bool dry = false) {
;     ...
;             for (int cq = 0; cq < 32; cq += 4) {
;                 f32x4 w4[4];
; #pragma unroll
;                 for (int k = 0; k < 4; ++k) w4[k] = *(const f32x4*)(wr + (size_t)(cq + k) * NE);
; #pragma unroll
;                 for (int r = 0; r < 8; ++r) { const f32x4 hv = *(const LAS f32x4*)(H2 + r * DM + cbase + cq);
; #pragma unroll
;                     for (int k = 0; k < 4; ++k) { const f32x2 hh = {hv[k], hv[k]}; acc[r][0] += hh * (f32x2){w4[k][0], w4[k][1]}; acc[r][1] += hh * (f32x2){w4[k][2], w4[k][3]}; } } }
	v_pk_fma_f32 v[14:15], v[6:7], v[164:165], v[22:23] op_sel_hi:[1,0,1]
	v_pk_fma_f32 v[16:17], v[8:9], v[164:165], v[18:19] op_sel_hi:[1,0,1]
	v_pk_fma_f32 v[18:19], v[6:7], v[166:167], v[20:21] op_sel_hi:[1,0,1]
	v_pk_fma_f32 v[20:21], v[8:9], v[166:167], v[24:25] op_sel_hi:[1,0,1]
	v_pk_fma_f32 v[22:23], v[6:7], v[168:169], v[38:39] op_sel_hi:[1,0,1]
	v_pk_fma_f32 v[24:25], v[8:9], v[168:169], v[68:69] op_sel_hi:[1,0,1]
	v_pk_fma_f32 v[38:39], v[6:7], v[170:171], v[70:71] op_sel_hi:[1,0,1]
	v_pk_fma_f32 v[52:53], v[8:9], v[170:171], v[52:53] op_sel_hi:[1,0,1]
	v_pk_fma_f32 v[50:51], v[6:7], v[172:173], v[50:51] op_sel_hi:[1,0,1]
	v_pk_fma_f32 v[48:49], v[8:9], v[172:173], v[48:49] op_sel_hi:[1,0,1]
	v_pk_fma_f32 v[46:47], v[6:7], v[174:175], v[46:47] op_sel_hi:[1,0,1]
	v_pk_fma_f32 v[44:45], v[8:9], v[174:175], v[44:45] op_sel_hi:[1,0,1]
	v_pk_fma_f32 v[42:43], v[6:7], v[176:177], v[42:43] op_sel_hi:[1,0,1]
	v_pk_fma_f32 v[40:41], v[8:9], v[176:177], v[40:41] op_sel_hi:[1,0,1]
	v_pk_fma_f32 v[6:7], v[6:7], v[178:179], v[10:11] op_sel_hi:[1,0,1]
	v_pk_fma_f32 v[8:9], v[8:9], v[178:179], v[12:13] op_sel_hi:[1,0,1]
	s_waitcnt vmcnt(3)
	v_pk_fma_f32 v[10:11], v[104:105], v[2:3], v[14:15] op_sel_hi:[1,0,1]
	v_pk_fma_f32 v[12:13], v[106:107], v[2:3], v[16:17] op_sel_hi:[1,0,1]
	v_pk_fma_f32 v[14:15], v[104:105], v[112:113], v[18:19] op_sel_hi:[1,0,1]
	v_pk_fma_f32 v[16:17], v[106:107], v[112:113], v[20:21] op_sel_hi:[1,0,1]
	v_pk_fma_f32 v[18:19], v[104:105], v[120:121], v[22:23] op_sel_hi:[1,0,1]
	v_pk_fma_f32 v[20:21], v[106:107], v[120:121], v[24:25] op_sel_hi:[1,0,1]
	v_pk_fma_f32 v[22:23], v[104:105], v[128:129], v[38:39] op_sel_hi:[1,0,1]
	v_pk_fma_f32 v[24:25], v[106:107], v[128:129], v[52:53] op_sel_hi:[1,0,1]
	v_pk_fma_f32 v[38:39], v[104:105], v[136:137], v[50:51] op_sel_hi:[1,0,1]
	v_pk_fma_f32 v[48:49], v[106:107], v[136:137], v[48:49] op_sel_hi:[1,0,1]
	v_pk_fma_f32 v[46:47], v[104:105], v[144:145], v[46:47] op_sel_hi:[1,0,1]
	v_pk_fma_f32 v[44:45], v[106:107], v[144:145], v[44:45] op_sel_hi:[1,0,1]
	v_pk_fma_f32 v[42:43], v[104:105], v[152:153], v[42:43] op_sel_hi:[1,0,1]
	v_pk_fma_f32 v[40:41], v[106:107], v[152:153], v[40:41] op_sel_hi:[1,0,1]
	v_pk_fma_f32 v[6:7], v[104:105], v[160:161], v[6:7] op_sel_hi:[1,0,1]
	v_pk_fma_f32 v[8:9], v[106:107], v[160:161], v[8:9] op_sel_hi:[1,0,1]
	s_waitcnt vmcnt(2)
	v_pk_fma_f32 v[10:11], v[34:35], v[2:3], v[10:11] op_sel:[0,1,0]
	v_pk_fma_f32 v[2:3], v[36:37], v[2:3], v[12:13] op_sel:[0,1,0]
	v_pk_fma_f32 v[12:13], v[34:35], v[112:113], v[14:15] op_sel:[0,1,0]
	v_pk_fma_f32 v[14:15], v[36:37], v[112:113], v[16:17] op_sel:[0,1,0]
	v_pk_fma_f32 v[16:17], v[34:35], v[120:121], v[18:19] op_sel:[0,1,0]
	v_pk_fma_f32 v[18:19], v[36:37], v[120:121], v[20:21] op_sel:[0,1,0]
	v_pk_fma_f32 v[20:21], v[34:35], v[128:129], v[22:23] op_sel:[0,1,0]
	v_pk_fma_f32 v[22:23], v[36:37], v[128:129], v[24:25] op_sel:[0,1,0]
	v_pk_fma_f32 v[24:25], v[34:35], v[136:137], v[38:39] op_sel:[0,1,0]
	v_pk_fma_f32 v[38:39], v[36:37], v[136:137], v[48:49] op_sel:[0,1,0]
	v_pk_fma_f32 v[46:47], v[34:35], v[144:145], v[46:47] op_sel:[0,1,0]
	v_pk_fma_f32 v[44:45], v[36:37], v[144:145], v[44:45] op_sel:[0,1,0]
	v_pk_fma_f32 v[42:43], v[34:35], v[152:153], v[42:43] op_sel:[0,1,0]
	v_pk_fma_f32 v[40:41], v[36:37], v[152:153], v[40:41] op_sel:[0,1,0]
	v_pk_fma_f32 v[6:7], v[34:35], v[160:161], v[6:7] op_sel:[0,1,0]
	v_pk_fma_f32 v[8:9], v[36:37], v[160:161], v[8:9] op_sel:[0,1,0]
	s_waitcnt vmcnt(1)
	v_pk_fma_f32 v[10:11], v[30:31], v[4:5], v[10:11] op_sel_hi:[1,0,1]
	v_pk_fma_f32 v[2:3], v[32:33], v[4:5], v[2:3] op_sel_hi:[1,0,1]
	v_pk_fma_f32 v[4:5], v[30:31], v[114:115], v[12:13] op_sel_hi:[1,0,1]
	v_pk_fma_f32 v[12:13], v[32:33], v[114:115], v[14:15] op_sel_hi:[1,0,1]
	v_pk_fma_f32 v[14:15], v[30:31], v[122:123], v[16:17] op_sel_hi:[1,0,1]
	v_pk_fma_f32 v[16:17], v[32:33], v[122:123], v[18:19] op_sel_hi:[1,0,1]
	v_pk_fma_f32 v[18:19], v[30:31], v[130:131], v[20:21] op_sel_hi:[1,0,1]
	v_pk_fma_f32 v[20:21], v[32:33], v[130:131], v[22:23] op_sel_hi:[1,0,1]
	v_pk_fma_f32 v[22:23], v[30:31], v[138:139], v[24:25] op_sel_hi:[1,0,1]
	v_pk_fma_f32 v[24:25], v[32:33], v[138:139], v[38:39] op_sel_hi:[1,0,1]
	v_pk_fma_f32 v[34:35], v[30:31], v[146:147], v[46:47] op_sel_hi:[1,0,1]
	v_pk_fma_f32 v[36:37], v[32:33], v[146:147], v[44:45] op_sel_hi:[1,0,1]
	v_pk_fma_f32 v[38:39], v[30:31], v[154:155], v[42:43] op_sel_hi:[1,0,1]
	v_pk_fma_f32 v[40:41], v[32:33], v[154:155], v[40:41] op_sel_hi:[1,0,1]
	v_pk_fma_f32 v[6:7], v[30:31], v[162:163], v[6:7] op_sel_hi:[1,0,1]
	v_pk_fma_f32 v[8:9], v[32:33], v[162:163], v[8:9] op_sel_hi:[1,0,1]
	s_waitcnt vmcnt(0)
	v_pk_fma_f32 v[84:85], v[26:27], v[180:181], v[10:11] op_sel_hi:[1,0,1]
	v_pk_fma_f32 v[82:83], v[28:29], v[180:181], v[2:3] op_sel_hi:[1,0,1]
	v_pk_fma_f32 v[80:81], v[26:27], v[182:183], v[4:5] op_sel_hi:[1,0,1]
	v_pk_fma_f32 v[78:79], v[28:29], v[182:183], v[12:13] op_sel_hi:[1,0,1]
	v_pk_fma_f32 v[76:77], v[26:27], v[184:185], v[14:15] op_sel_hi:[1,0,1]
	v_pk_fma_f32 v[72:73], v[28:29], v[184:185], v[16:17] op_sel_hi:[1,0,1]
	v_pk_fma_f32 v[70:71], v[26:27], v[186:187], v[18:19] op_sel_hi:[1,0,1]
	v_pk_fma_f32 v[52:53], v[28:29], v[186:187], v[20:21] op_sel_hi:[1,0,1]
	v_pk_fma_f32 v[50:51], v[26:27], v[188:189], v[22:23] op_sel_hi:[1,0,1]
	v_pk_fma_f32 v[48:49], v[28:29], v[188:189], v[24:25] op_sel_hi:[1,0,1]
	v_pk_fma_f32 v[46:47], v[26:27], v[190:191], v[34:35] op_sel_hi:[1,0,1]
	v_pk_fma_f32 v[44:45], v[28:29], v[190:191], v[36:37] op_sel_hi:[1,0,1]
	v_pk_fma_f32 v[42:43], v[26:27], v[192:193], v[38:39] op_sel_hi:[1,0,1]
	v_pk_fma_f32 v[40:41], v[28:29], v[192:193], v[40:41] op_sel_hi:[1,0,1]
	v_pk_fma_f32 v[38:39], v[26:27], v[194:195], v[6:7] op_sel_hi:[1,0,1]
	v_pk_fma_f32 v[68:69], v[28:29], v[194:195], v[8:9] op_sel_hi:[1,0,1]
	s_cbranch_scc0 .LBB0_1218
; template <int CTRL> __device__ __forceinline__ float dpp_f(float x) { return __int_as_float(__builtin_amdgcn_update_dpp(0, __float_as_int(x), CTRL, 0xF, 0xF, true)); }
; __device__ __forceinline__ float xor16_sum(float x) { const auto r = __builtin_amdgcn_permlane16_swap(__float_as_uint(x), __float_as_uint(x), false, false); return __uint_as_float(r[0]) + __uint_as_float(r[1]); }
; __device__ __forceinline__ float xor32_sum(float x) { const auto r = __builtin_amdgcn_permlane32_swap(__float_as_uint(x), __float_as_uint(x), false, false); return __uint_as_float(r[0]) + __uint_as_float(r[1]); }
; __device__ __forceinline__ void ph_post1(Ctx& C, int l, int nrows, bool dry = false) {
;     ...
; #pragma unroll
;             for (int r = 0; r < 8; ++r)
; #pragma unroll
;                 for (int k = 0; k < 2; ++k) { float x = acc[r][k].x, y = acc[r][k].y;
;                     x += dpp_f<DPP_ROR8>(x); y += dpp_f<DPP_ROR8>(y); x = xor32_sum(xor16_sum(x)); y = xor32_sum(xor16_sum(y));
;                     if (cg == 0) { RED[(C.wave * 8 + r) * 32 + 4 * e4 + 2 * k] = x; RED[(C.wave * 8 + r) * 32 + 4 * e4 + 2 * k + 1] = y; } }
;         }
;         __syncthreads();
;         if (C.tid < 256) { const int r = C.tid >> 5, e = C.tid & 31; float s = 0.f;
; #pragma unroll
;             for (int p = 0; p < 8; ++p) s += RED[(p * 8 + r) * 32 + e];
;             SGA[(nit * 8 + r) * 32 + e] = 1.0f / (1.0f + expf(-s)); }
	s_nop 1
	v_add_f32_dpp v84, v84, v84 row_ror:8 row_mask:0xf bank_mask:0xf bound_ctrl:1
	v_add_f32_dpp v85, v85, v85 row_ror:8 row_mask:0xf bank_mask:0xf bound_ctrl:1
	v_add_f32_dpp v82, v82, v82 row_ror:8 row_mask:0xf bank_mask:0xf bound_ctrl:1
	v_add_f32_dpp v83, v83, v83 row_ror:8 row_mask:0xf bank_mask:0xf bound_ctrl:1
	v_add_f32_dpp v80, v80, v80 row_ror:8 row_mask:0xf bank_mask:0xf bound_ctrl:1
	v_add_f32_dpp v81, v81, v81 row_ror:8 row_mask:0xf bank_mask:0xf bound_ctrl:1
	v_add_f32_dpp v78, v78, v78 row_ror:8 row_mask:0xf bank_mask:0xf bound_ctrl:1
	v_add_f32_dpp v79, v79, v79 row_ror:8 row_mask:0xf bank_mask:0xf bound_ctrl:1
	v_add_f32_dpp v76, v76, v76 row_ror:8 row_mask:0xf bank_mask:0xf bound_ctrl:1
	v_add_f32_dpp v77, v77, v77 row_ror:8 row_mask:0xf bank_mask:0xf bound_ctrl:1
	v_add_f32_dpp v72, v72, v72 row_ror:8 row_mask:0xf bank_mask:0xf bound_ctrl:1
	v_add_f32_dpp v73, v73, v73 row_ror:8 row_mask:0xf bank_mask:0xf bound_ctrl:1
	v_add_f32_dpp v70, v70, v70 row_ror:8 row_mask:0xf bank_mask:0xf bound_ctrl:1
	v_add_f32_dpp v71, v71, v71 row_ror:8 row_mask:0xf bank_mask:0xf bound_ctrl:1
	v_add_f32_dpp v52, v52, v52 row_ror:8 row_mask:0xf bank_mask:0xf bound_ctrl:1
	v_add_f32_dpp v53, v53, v53 row_ror:8 row_mask:0xf bank_mask:0xf bound_ctrl:1
	v_add_f32_dpp v50, v50, v50 row_ror:8 row_mask:0xf bank_mask:0xf bound_ctrl:1
	v_add_f32_dpp v51, v51, v51 row_ror:8 row_mask:0xf bank_mask:0xf bound_ctrl:1
	v_add_f32_dpp v48, v48, v48 row_ror:8 row_mask:0xf bank_mask:0xf bound_ctrl:1
	v_add_f32_dpp v49, v49, v49 row_ror:8 row_mask:0xf bank_mask:0xf bound_ctrl:1
	v_add_f32_dpp v46, v46, v46 row_ror:8 row_mask:0xf bank_mask:0xf bound_ctrl:1
	v_add_f32_dpp v47, v47, v47 row_ror:8 row_mask:0xf bank_mask:0xf bound_ctrl:1
	v_add_f32_dpp v44, v44, v44 row_ror:8 row_mask:0xf bank_mask:0xf bound_ctrl:1
	v_add_f32_dpp v45, v45, v45 row_ror:8 row_mask:0xf bank_mask:0xf bound_ctrl:1
	v_add_f32_dpp v42, v42, v42 row_ror:8 row_mask:0xf bank_mask:0xf bound_ctrl:1
	v_add_f32_dpp v43, v43, v43 row_ror:8 row_mask:0xf bank_mask:0xf bound_ctrl:1
	v_add_f32_dpp v40, v40, v40 row_ror:8 row_mask:0xf bank_mask:0xf bound_ctrl:1
	v_add_f32_dpp v41, v41, v41 row_ror:8 row_mask:0xf bank_mask:0xf bound_ctrl:1
	v_add_f32_dpp v38, v38, v38 row_ror:8 row_mask:0xf bank_mask:0xf bound_ctrl:1
	v_add_f32_dpp v39, v39, v39 row_ror:8 row_mask:0xf bank_mask:0xf bound_ctrl:1
	v_add_f32_dpp v68, v68, v68 row_ror:8 row_mask:0xf bank_mask:0xf bound_ctrl:1
	v_add_f32_dpp v69, v69, v69 row_ror:8 row_mask:0xf bank_mask:0xf bound_ctrl:1
	v_permlane16_swap_b32_e32 v84, v50
	v_permlane16_swap_b32_e32 v85, v51
	v_permlane16_swap_b32_e32 v82, v48
	v_permlane16_swap_b32_e32 v83, v49
	v_permlane16_swap_b32_e32 v80, v46
	v_permlane16_swap_b32_e32 v81, v47
	v_permlane16_swap_b32_e32 v78, v44
	v_permlane16_swap_b32_e32 v79, v45
	v_permlane16_swap_b32_e32 v76, v42
	v_permlane16_swap_b32_e32 v77, v43
	v_permlane16_swap_b32_e32 v72, v40
	v_permlane16_swap_b32_e32 v73, v41
	v_permlane16_swap_b32_e32 v70, v38
	v_permlane16_swap_b32_e32 v71, v39
	v_permlane16_swap_b32_e32 v52, v68
	v_permlane16_swap_b32_e32 v53, v69
	v_add_f32_e32 v84, v84, v50
	v_add_f32_e32 v85, v85, v51
	v_add_f32_e32 v82, v82, v48
	v_add_f32_e32 v83, v83, v49
	v_add_f32_e32 v80, v80, v46
	v_add_f32_e32 v81, v81, v47
	v_add_f32_e32 v78, v78, v44
	v_add_f32_e32 v79, v79, v45
	v_add_f32_e32 v76, v76, v42
	v_add_f32_e32 v77, v77, v43
	v_add_f32_e32 v72, v72, v40
	v_add_f32_e32 v73, v73, v41
	v_add_f32_e32 v70, v70, v38
	v_add_f32_e32 v71, v71, v39
	v_add_f32_e32 v52, v52, v68
	v_add_f32_e32 v53, v53, v69
	v_permlane32_swap_b32_e32 v84, v76
	v_permlane32_swap_b32_e32 v85, v77
	v_permlane32_swap_b32_e32 v82, v72
	v_permlane32_swap_b32_e32 v83, v73
	v_permlane32_swap_b32_e32 v80, v70
	v_permlane32_swap_b32_e32 v81, v71
	v_permlane32_swap_b32_e32 v78, v52
	v_permlane32_swap_b32_e32 v79, v53
	v_mbcnt_lo_u32_b32 v10, -1, 0
	v_mbcnt_hi_u32_b32 v10, -1, v10
	v_and_b32_e32 v11, 7, v10
	v_lshlrev_b32_e32 v11, 4, v11
	v_bfe_u32 v12, v10, 4, 1
	v_lshl_add_u32 v11, v12, 9, v11
	v_bfe_u32 v12, v10, 5, 1
	v_lshl_add_u32 v11, v12, 8, v11
	v_add_f32_e32 v2, v84, v76
	v_add_f32_e32 v3, v85, v77
	v_add_f32_e32 v4, v82, v72
	v_add_f32_e32 v5, v83, v73
	v_add_f32_e32 v6, v80, v70
	v_add_f32_e32 v7, v81, v71
	v_add_f32_e32 v8, v78, v52
	v_add_f32_e32 v9, v79, v53
	v_readfirstlane_b32 s8, v55
	s_nop 1
	v_add_u32_e32 v11, s8, v11
	ds_write_b128 v11, v[2:5]
	ds_write_b128 v11, v[6:9] offset:128
	s_waitcnt lgkmcnt(0)
	s_barrier
	s_and_saveexec_b64 s[8:9], s[6:7]
	s_cbranch_execz .LBB0_1214
	ds_read2st64_b32 v[2:3], v91 offset1:4
	ds_read2st64_b32 v[4:5], v91 offset0:8 offset1:12
	ds_read2st64_b32 v[6:7], v91 offset0:16 offset1:20
	ds_read2st64_b32 v[8:9], v91 offset0:24 offset1:28
	s_waitcnt lgkmcnt(3)
	v_add_f32_e32 v2, 0, v2
	v_add_f32_e32 v2, v2, v3
	s_waitcnt lgkmcnt(2)
	v_add_f32_e32 v2, v2, v4
	v_add_f32_e32 v2, v2, v5
	s_waitcnt lgkmcnt(1)
	v_add_f32_e32 v2, v2, v6
	v_add_f32_e32 v2, v2, v7
	s_waitcnt lgkmcnt(0)
	v_add_f32_e32 v2, v2, v8
	v_add_f32_e32 v2, v2, v9
	v_mul_f32_e32 v3, 0xbfb8aa3b, v2
	v_fma_f32 v4, v2, s35, -v3
	v_rndne_f32_e32 v5, v3
	v_fmac_f32_e32 v4, 0xb2a5705f, v2
	v_sub_f32_e32 v3, v3, v5
	v_add_f32_e32 v3, v3, v4
	v_cvt_i32_f32_e32 v4, v5
	v_exp_f32_e32 v3, v3
	v_cmp_nlt_f32_e32 vcc, s44, v2
	v_ldexp_f32 v3, v3, v4
	s_nop 0
	v_cndmask_b32_e32 v3, 0, v3, vcc
	v_cmp_ngt_f32_e32 vcc, s45, v2
	s_nop 1
	v_cndmask_b32_e32 v2, v101, v3, vcc
	v_add_f32_e32 v2, 1.0, v2
	v_div_scale_f32 v3, s[38:39], v2, v2, 1.0
	v_rcp_f32_e32 v4, v3
	s_nop 0
	v_fma_f32 v5, -v3, v4, 1.0
	v_fmac_f32_e32 v4, v5, v4
	v_div_scale_f32 v5, vcc, 1.0, v2, 1.0
	v_mul_f32_e32 v6, v5, v4
	v_fma_f32 v7, -v3, v6, v5
	v_fmac_f32_e32 v6, v7, v4
	v_fma_f32 v3, -v3, v6, v5
	v_div_fmas_f32 v3, v3, v4, v6
	v_div_fixup_f32 v2, v3, v2, 1.0
	v_lshl_add_u32 v3, s13, 10, v92
	ds_write_b32 v3, v2
	s_branch .LBB0_1214

; #define LAS __attribute__((address_space(3)))
; __device__ __forceinline__ void ph_post1(Ctx& C, int l, int nrows, bool dry = false) {
;     ...
; #pragma unroll 2
;             for (int cq = 0; cq < 32; cq += 4) {
;                 f32x4 w4[4];
; #pragma unroll
;                 for (int k = 0; k < 4; ++k) w4[k] = *(const f32x4*)(wr + (size_t)(cq + k) * NE);
; #pragma unroll
;                 for (int r = 0; r < 8; ++r) { const f32x4 hv = *(const LAS f32x4*)(H2 + r * DM + cbase + cq);
; #pragma unroll
;                     for (int k = 0; k < 4; ++k) { const f32x2 hh = {hv[k], hv[k]}; acc[r][0] += hh * (f32x2){w4[k][0], w4[k][1]}; acc[r][1] += hh * (f32x2){w4[k][2], w4[k][3]}; } } }
.LBB0_2353:
	global_load_dwordx4 v[22:25], v[58:59], off offset:-896
	global_load_dwordx4 v[14:17], v[58:59], off offset:-768
	global_load_dwordx4 v[10:13], v[58:59], off offset:-640
	global_load_dwordx4 v[6:9], v[58:59], off offset:-512
	ds_read_b128 v[18:21], v84
	ds_read_b128 v[2:5], v84 offset:16
	global_load_dwordx4 v[86:89], v[58:59], off offset:-384
	global_load_dwordx4 v[34:37], v[58:59], off offset:-256
	global_load_dwordx4 v[30:33], v[58:59], off offset:-128
	global_load_dwordx4 v[26:29], v[58:59], off
	ds_read_b128 v[90:93], v84 offset:8192
	ds_read_b128 v[110:113], v84 offset:8208
	ds_read_b128 v[114:117], v84 offset:16384
	ds_read_b128 v[118:121], v84 offset:16400
	ds_read_b128 v[122:125], v84 offset:24576
	ds_read_b128 v[126:129], v84 offset:24592
	ds_read_b128 v[130:133], v84 offset:32768
	ds_read_b128 v[134:137], v84 offset:32784
	ds_read_b128 v[138:141], v84 offset:40960
	ds_read_b128 v[142:145], v84 offset:40976
	ds_read_b128 v[146:149], v84 offset:49152
	ds_read_b128 v[150:153], v84 offset:49168
	ds_read_b128 v[154:157], v84 offset:57344
	ds_read_b128 v[158:161], v84 offset:57360
	s_waitcnt lgkmcnt(13)
	v_mov_b32_e32 v164, v93
	v_mov_b32_e32 v162, v21
	s_waitcnt lgkmcnt(11)
	v_mov_b32_e32 v166, v117
	s_waitcnt lgkmcnt(9)
	v_mov_b32_e32 v168, v125
	s_waitcnt lgkmcnt(7)
	v_mov_b32_e32 v170, v133
	s_waitcnt lgkmcnt(5)
	v_mov_b32_e32 v172, v141
	s_waitcnt lgkmcnt(3)
	v_mov_b32_e32 v174, v149
	s_waitcnt lgkmcnt(1)
	v_mov_b32_e32 v176, v157
	s_add_i32 s8, s8, 8
	v_mov_b32_e32 v178, v5
	v_mov_b32_e32 v180, v113
	v_mov_b32_e32 v182, v121
	v_mov_b32_e32 v184, v129
	v_mov_b32_e32 v186, v137
	v_mov_b32_e32 v188, v145
	v_mov_b32_e32 v190, v153
	s_waitcnt lgkmcnt(0)
	v_mov_b32_e32 v192, v161
	v_lshl_add_u64 v[58:59], v[58:59], 0, s[24:25]
	v_add_u32_e32 v84, 32, v84
	s_cmp_gt_u32 s8, 27
	s_waitcnt vmcnt(7)
	v_pk_fma_f32 v[82:83], v[22:23], v[18:19], v[82:83] op_sel_hi:[1,0,1]
	v_pk_fma_f32 v[80:81], v[24:25], v[18:19], v[80:81] op_sel_hi:[1,0,1]
	v_pk_fma_f32 v[78:79], v[22:23], v[90:91], v[78:79] op_sel_hi:[1,0,1]
	v_pk_fma_f32 v[76:77], v[24:25], v[90:91], v[76:77] op_sel_hi:[1,0,1]
	v_pk_fma_f32 v[60:61], v[22:23], v[114:115], v[60:61] op_sel_hi:[1,0,1]
	v_pk_fma_f32 v[56:57], v[24:25], v[114:115], v[56:57] op_sel_hi:[1,0,1]
	v_pk_fma_f32 v[54:55], v[22:23], v[122:123], v[54:55] op_sel_hi:[1,0,1]
	v_pk_fma_f32 v[52:53], v[24:25], v[122:123], v[52:53] op_sel_hi:[1,0,1]
	v_pk_fma_f32 v[50:51], v[22:23], v[130:131], v[50:51] op_sel_hi:[1,0,1]
	v_pk_fma_f32 v[48:49], v[24:25], v[130:131], v[48:49] op_sel_hi:[1,0,1]
	v_pk_fma_f32 v[46:47], v[22:23], v[138:139], v[46:47] op_sel_hi:[1,0,1]
	v_pk_fma_f32 v[44:45], v[24:25], v[138:139], v[44:45] op_sel_hi:[1,0,1]
	v_pk_fma_f32 v[42:43], v[22:23], v[146:147], v[42:43] op_sel_hi:[1,0,1]
	v_pk_fma_f32 v[40:41], v[24:25], v[146:147], v[40:41] op_sel_hi:[1,0,1]
	v_pk_fma_f32 v[22:23], v[22:23], v[154:155], v[38:39] op_sel_hi:[1,0,1]
	v_pk_fma_f32 v[24:25], v[24:25], v[154:155], v[74:75] op_sel_hi:[1,0,1]
	s_waitcnt vmcnt(6)
	v_pk_fma_f32 v[38:39], v[14:15], v[18:19], v[82:83] op_sel:[0,1,0]
	v_pk_fma_f32 v[18:19], v[16:17], v[18:19], v[80:81] op_sel:[0,1,0]
	v_pk_fma_f32 v[74:75], v[14:15], v[90:91], v[78:79] op_sel:[0,1,0]
	v_pk_fma_f32 v[76:77], v[16:17], v[90:91], v[76:77] op_sel:[0,1,0]
	v_pk_fma_f32 v[60:61], v[14:15], v[114:115], v[60:61] op_sel:[0,1,0]
	v_pk_fma_f32 v[56:57], v[16:17], v[114:115], v[56:57] op_sel:[0,1,0]
	v_pk_fma_f32 v[54:55], v[14:15], v[122:123], v[54:55] op_sel:[0,1,0]
	v_pk_fma_f32 v[52:53], v[16:17], v[122:123], v[52:53] op_sel:[0,1,0]
	v_pk_fma_f32 v[50:51], v[14:15], v[130:131], v[50:51] op_sel:[0,1,0]
	v_pk_fma_f32 v[48:49], v[16:17], v[130:131], v[48:49] op_sel:[0,1,0]
	v_pk_fma_f32 v[46:47], v[14:15], v[138:139], v[46:47] op_sel:[0,1,0]
	v_pk_fma_f32 v[44:45], v[16:17], v[138:139], v[44:45] op_sel:[0,1,0]
	v_pk_fma_f32 v[42:43], v[14:15], v[146:147], v[42:43] op_sel:[0,1,0]
	v_pk_fma_f32 v[40:41], v[16:17], v[146:147], v[40:41] op_sel:[0,1,0]
	v_pk_fma_f32 v[14:15], v[14:15], v[154:155], v[22:23] op_sel:[0,1,0]
	v_pk_fma_f32 v[16:17], v[16:17], v[154:155], v[24:25] op_sel:[0,1,0]
	s_waitcnt vmcnt(5)
	v_pk_fma_f32 v[22:23], v[10:11], v[20:21], v[38:39] op_sel_hi:[1,0,1]
	v_pk_fma_f32 v[18:19], v[12:13], v[20:21], v[18:19] op_sel_hi:[1,0,1]
	v_pk_fma_f32 v[20:21], v[10:11], v[92:93], v[74:75] op_sel_hi:[1,0,1]
	v_pk_fma_f32 v[24:25], v[12:13], v[92:93], v[76:77] op_sel_hi:[1,0,1]
	v_pk_fma_f32 v[38:39], v[10:11], v[116:117], v[60:61] op_sel_hi:[1,0,1]
	v_pk_fma_f32 v[56:57], v[12:13], v[116:117], v[56:57] op_sel_hi:[1,0,1]
	v_pk_fma_f32 v[54:55], v[10:11], v[124:125], v[54:55] op_sel_hi:[1,0,1]
	v_pk_fma_f32 v[52:53], v[12:13], v[124:125], v[52:53] op_sel_hi:[1,0,1]
	v_pk_fma_f32 v[50:51], v[10:11], v[132:133], v[50:51] op_sel_hi:[1,0,1]
	v_pk_fma_f32 v[48:49], v[12:13], v[132:133], v[48:49] op_sel_hi:[1,0,1]
	v_pk_fma_f32 v[46:47], v[10:11], v[140:141], v[46:47] op_sel_hi:[1,0,1]
	v_pk_fma_f32 v[44:45], v[12:13], v[140:141], v[44:45] op_sel_hi:[1,0,1]
	v_pk_fma_f32 v[42:43], v[10:11], v[148:149], v[42:43] op_sel_hi:[1,0,1]
	v_pk_fma_f32 v[40:41], v[12:13], v[148:149], v[40:41] op_sel_hi:[1,0,1]
	v_pk_fma_f32 v[10:11], v[10:11], v[156:157], v[14:15] op_sel_hi:[1,0,1]
	v_pk_fma_f32 v[12:13], v[12:13], v[156:157], v[16:17] op_sel_hi:[1,0,1]
	s_waitcnt vmcnt(4)
; #define LAS __attribute__((address_space(3)))
; __device__ __forceinline__ void ph_post1(Ctx& C, int l, int nrows, bool dry = false) {
;     ...
;             for (int cq = 0; cq < 32; cq += 4) {
;                 f32x4 w4[4];
; #pragma unroll
;                 for (int k = 0; k < 4; ++k) w4[k] = *(const f32x4*)(wr + (size_t)(cq + k) * NE);
; #pragma unroll
;                 for (int r = 0; r < 8; ++r) { const f32x4 hv = *(const LAS f32x4*)(H2 + r * DM + cbase + cq);
; #pragma unroll
;                     for (int k = 0; k < 4; ++k) { const f32x2 hh = {hv[k], hv[k]}; acc[r][0] += hh * (f32x2){w4[k][0], w4[k][1]}; acc[r][1] += hh * (f32x2){w4[k][2], w4[k][3]}; } } }
	v_pk_fma_f32 v[14:15], v[6:7], v[162:163], v[22:23] op_sel_hi:[1,0,1]
	v_pk_fma_f32 v[16:17], v[8:9], v[162:163], v[18:19] op_sel_hi:[1,0,1]
	v_pk_fma_f32 v[18:19], v[6:7], v[164:165], v[20:21] op_sel_hi:[1,0,1]
	v_pk_fma_f32 v[20:21], v[8:9], v[164:165], v[24:25] op_sel_hi:[1,0,1]
	v_pk_fma_f32 v[22:23], v[6:7], v[166:167], v[38:39] op_sel_hi:[1,0,1]
	v_pk_fma_f32 v[24:25], v[8:9], v[166:167], v[56:57] op_sel_hi:[1,0,1]
	v_pk_fma_f32 v[38:39], v[6:7], v[168:169], v[54:55] op_sel_hi:[1,0,1]
	v_pk_fma_f32 v[52:53], v[8:9], v[168:169], v[52:53] op_sel_hi:[1,0,1]
	v_pk_fma_f32 v[50:51], v[6:7], v[170:171], v[50:51] op_sel_hi:[1,0,1]
	v_pk_fma_f32 v[48:49], v[8:9], v[170:171], v[48:49] op_sel_hi:[1,0,1]
	v_pk_fma_f32 v[46:47], v[6:7], v[172:173], v[46:47] op_sel_hi:[1,0,1]
	v_pk_fma_f32 v[44:45], v[8:9], v[172:173], v[44:45] op_sel_hi:[1,0,1]
	v_pk_fma_f32 v[42:43], v[6:7], v[174:175], v[42:43] op_sel_hi:[1,0,1]
	v_pk_fma_f32 v[40:41], v[8:9], v[174:175], v[40:41] op_sel_hi:[1,0,1]
	v_pk_fma_f32 v[6:7], v[6:7], v[176:177], v[10:11] op_sel_hi:[1,0,1]
	v_pk_fma_f32 v[8:9], v[8:9], v[176:177], v[12:13] op_sel_hi:[1,0,1]
	s_waitcnt vmcnt(3)
	v_pk_fma_f32 v[10:11], v[86:87], v[2:3], v[14:15] op_sel_hi:[1,0,1]
	v_pk_fma_f32 v[12:13], v[88:89], v[2:3], v[16:17] op_sel_hi:[1,0,1]
	v_pk_fma_f32 v[14:15], v[86:87], v[110:111], v[18:19] op_sel_hi:[1,0,1]
	v_pk_fma_f32 v[16:17], v[88:89], v[110:111], v[20:21] op_sel_hi:[1,0,1]
	v_pk_fma_f32 v[18:19], v[86:87], v[118:119], v[22:23] op_sel_hi:[1,0,1]
	v_pk_fma_f32 v[20:21], v[88:89], v[118:119], v[24:25] op_sel_hi:[1,0,1]
	v_pk_fma_f32 v[22:23], v[86:87], v[126:127], v[38:39] op_sel_hi:[1,0,1]
	v_pk_fma_f32 v[24:25], v[88:89], v[126:127], v[52:53] op_sel_hi:[1,0,1]
	v_pk_fma_f32 v[38:39], v[86:87], v[134:135], v[50:51] op_sel_hi:[1,0,1]
	v_pk_fma_f32 v[48:49], v[88:89], v[134:135], v[48:49] op_sel_hi:[1,0,1]
	v_pk_fma_f32 v[46:47], v[86:87], v[142:143], v[46:47] op_sel_hi:[1,0,1]
	v_pk_fma_f32 v[44:45], v[88:89], v[142:143], v[44:45] op_sel_hi:[1,0,1]
	v_pk_fma_f32 v[42:43], v[86:87], v[150:151], v[42:43] op_sel_hi:[1,0,1]
	v_pk_fma_f32 v[40:41], v[88:89], v[150:151], v[40:41] op_sel_hi:[1,0,1]
	v_pk_fma_f32 v[6:7], v[86:87], v[158:159], v[6:7] op_sel_hi:[1,0,1]
	v_pk_fma_f32 v[8:9], v[88:89], v[158:159], v[8:9] op_sel_hi:[1,0,1]
	s_waitcnt vmcnt(2)
	v_pk_fma_f32 v[10:11], v[34:35], v[2:3], v[10:11] op_sel:[0,1,0]
	v_pk_fma_f32 v[2:3], v[36:37], v[2:3], v[12:13] op_sel:[0,1,0]
	v_pk_fma_f32 v[12:13], v[34:35], v[110:111], v[14:15] op_sel:[0,1,0]
	v_pk_fma_f32 v[14:15], v[36:37], v[110:111], v[16:17] op_sel:[0,1,0]
	v_pk_fma_f32 v[16:17], v[34:35], v[118:119], v[18:19] op_sel:[0,1,0]
	v_pk_fma_f32 v[18:19], v[36:37], v[118:119], v[20:21] op_sel:[0,1,0]
	v_pk_fma_f32 v[20:21], v[34:35], v[126:127], v[22:23] op_sel:[0,1,0]
	v_pk_fma_f32 v[22:23], v[36:37], v[126:127], v[24:25] op_sel:[0,1,0]
	v_pk_fma_f32 v[24:25], v[34:35], v[134:135], v[38:39] op_sel:[0,1,0]
	v_pk_fma_f32 v[38:39], v[36:37], v[134:135], v[48:49] op_sel:[0,1,0]
	v_pk_fma_f32 v[46:47], v[34:35], v[142:143], v[46:47] op_sel:[0,1,0]
	v_pk_fma_f32 v[44:45], v[36:37], v[142:143], v[44:45] op_sel:[0,1,0]
	v_pk_fma_f32 v[42:43], v[34:35], v[150:151], v[42:43] op_sel:[0,1,0]
	v_pk_fma_f32 v[40:41], v[36:37], v[150:151], v[40:41] op_sel:[0,1,0]
	v_pk_fma_f32 v[6:7], v[34:35], v[158:159], v[6:7] op_sel:[0,1,0]
	v_pk_fma_f32 v[8:9], v[36:37], v[158:159], v[8:9] op_sel:[0,1,0]
	s_waitcnt vmcnt(1)
	v_pk_fma_f32 v[10:11], v[30:31], v[4:5], v[10:11] op_sel_hi:[1,0,1]
	v_pk_fma_f32 v[2:3], v[32:33], v[4:5], v[2:3] op_sel_hi:[1,0,1]
	v_pk_fma_f32 v[4:5], v[30:31], v[112:113], v[12:13] op_sel_hi:[1,0,1]
	v_pk_fma_f32 v[12:13], v[32:33], v[112:113], v[14:15] op_sel_hi:[1,0,1]
	v_pk_fma_f32 v[14:15], v[30:31], v[120:121], v[16:17] op_sel_hi:[1,0,1]
	v_pk_fma_f32 v[16:17], v[32:33], v[120:121], v[18:19] op_sel_hi:[1,0,1]
	v_pk_fma_f32 v[18:19], v[30:31], v[128:129], v[20:21] op_sel_hi:[1,0,1]
	v_pk_fma_f32 v[20:21], v[32:33], v[128:129], v[22:23] op_sel_hi:[1,0,1]
	v_pk_fma_f32 v[22:23], v[30:31], v[136:137], v[24:25] op_sel_hi:[1,0,1]
	v_pk_fma_f32 v[24:25], v[32:33], v[136:137], v[38:39] op_sel_hi:[1,0,1]
	v_pk_fma_f32 v[34:35], v[30:31], v[144:145], v[46:47] op_sel_hi:[1,0,1]
	v_pk_fma_f32 v[36:37], v[32:33], v[144:145], v[44:45] op_sel_hi:[1,0,1]
	v_pk_fma_f32 v[38:39], v[30:31], v[152:153], v[42:43] op_sel_hi:[1,0,1]
	v_pk_fma_f32 v[40:41], v[32:33], v[152:153], v[40:41] op_sel_hi:[1,0,1]
	v_pk_fma_f32 v[6:7], v[30:31], v[160:161], v[6:7] op_sel_hi:[1,0,1]
	v_pk_fma_f32 v[8:9], v[32:33], v[160:161], v[8:9] op_sel_hi:[1,0,1]
	s_waitcnt vmcnt(0)
	v_pk_fma_f32 v[82:83], v[26:27], v[178:179], v[10:11] op_sel_hi:[1,0,1]
	v_pk_fma_f32 v[80:81], v[28:29], v[178:179], v[2:3] op_sel_hi:[1,0,1]
	v_pk_fma_f32 v[78:79], v[26:27], v[180:181], v[4:5] op_sel_hi:[1,0,1]
	v_pk_fma_f32 v[76:77], v[28:29], v[180:181], v[12:13] op_sel_hi:[1,0,1]
	v_pk_fma_f32 v[60:61], v[26:27], v[182:183], v[14:15] op_sel_hi:[1,0,1]
	v_pk_fma_f32 v[56:57], v[28:29], v[182:183], v[16:17] op_sel_hi:[1,0,1]
	v_pk_fma_f32 v[54:55], v[26:27], v[184:185], v[18:19] op_sel_hi:[1,0,1]
	v_pk_fma_f32 v[52:53], v[28:29], v[184:185], v[20:21] op_sel_hi:[1,0,1]
	v_pk_fma_f32 v[50:51], v[26:27], v[186:187], v[22:23] op_sel_hi:[1,0,1]
	v_pk_fma_f32 v[48:49], v[28:29], v[186:187], v[24:25] op_sel_hi:[1,0,1]
	v_pk_fma_f32 v[46:47], v[26:27], v[188:189], v[34:35] op_sel_hi:[1,0,1]
	v_pk_fma_f32 v[44:45], v[28:29], v[188:189], v[36:37] op_sel_hi:[1,0,1]
	v_pk_fma_f32 v[42:43], v[26:27], v[190:191], v[38:39] op_sel_hi:[1,0,1]
	v_pk_fma_f32 v[40:41], v[28:29], v[190:191], v[40:41] op_sel_hi:[1,0,1]
	v_pk_fma_f32 v[38:39], v[26:27], v[192:193], v[6:7] op_sel_hi:[1,0,1]
	v_pk_fma_f32 v[74:75], v[28:29], v[192:193], v[8:9] op_sel_hi:[1,0,1]
	s_cbranch_scc0 .LBB0_2353
; template <int CTRL> __device__ __forceinline__ float dpp_f(float x) { return __int_as_float(__builtin_amdgcn_update_dpp(0, __float_as_int(x), CTRL, 0xF, 0xF, true)); }
; __device__ __forceinline__ float xor16_sum(float x) { const auto r = __builtin_amdgcn_permlane16_swap(__float_as_uint(x), __float_as_uint(x), false, false); return __uint_as_float(r[0]) + __uint_as_float(r[1]); }
; __device__ __forceinline__ float xor32_sum(float x) { const auto r = __builtin_amdgcn_permlane32_swap(__float_as_uint(x), __float_as_uint(x), false, false); return __uint_as_float(r[0]) + __uint_as_float(r[1]); }
; __device__ __forceinline__ void ph_post1(Ctx& C, int l, int nrows, bool dry = false) {
;     ...
; #pragma unroll
;             for (int r = 0; r < 8; ++r)
; #pragma unroll
;                 for (int k = 0; k < 2; ++k) { float x = acc[r][k].x, y = acc[r][k].y;
;                     x += dpp_f<DPP_ROR8>(x); y += dpp_f<DPP_ROR8>(y); x = xor32_sum(xor16_sum(x)); y = xor32_sum(xor16_sum(y));
;                     if (cg == 0) { RED[(C.wave * 8 + r) * 32 + 4 * e4 + 2 * k] = x; RED[(C.wave * 8 + r) * 32 + 4 * e4 + 2 * k + 1] = y; } }
;         }
;         __syncthreads();
;         if (C.tid < 256) { const int r = C.tid >> 5, e = C.tid & 31; float s = 0.f;
; #pragma unroll
;             for (int p = 0; p < 8; ++p) s += RED[(p * 8 + r) * 32 + e];
;             SGA[(nit * 8 + r) * 32 + e] = 1.0f / (1.0f + expf(-s)); }
	s_nop 1
	v_add_f32_dpp v82, v82, v82 row_ror:8 row_mask:0xf bank_mask:0xf bound_ctrl:1
	v_add_f32_dpp v83, v83, v83 row_ror:8 row_mask:0xf bank_mask:0xf bound_ctrl:1
	v_add_f32_dpp v80, v80, v80 row_ror:8 row_mask:0xf bank_mask:0xf bound_ctrl:1
	v_add_f32_dpp v81, v81, v81 row_ror:8 row_mask:0xf bank_mask:0xf bound_ctrl:1
	v_add_f32_dpp v78, v78, v78 row_ror:8 row_mask:0xf bank_mask:0xf bound_ctrl:1
	v_add_f32_dpp v79, v79, v79 row_ror:8 row_mask:0xf bank_mask:0xf bound_ctrl:1
	v_add_f32_dpp v76, v76, v76 row_ror:8 row_mask:0xf bank_mask:0xf bound_ctrl:1
	v_add_f32_dpp v77, v77, v77 row_ror:8 row_mask:0xf bank_mask:0xf bound_ctrl:1
	v_add_f32_dpp v60, v60, v60 row_ror:8 row_mask:0xf bank_mask:0xf bound_ctrl:1
	v_add_f32_dpp v61, v61, v61 row_ror:8 row_mask:0xf bank_mask:0xf bound_ctrl:1
	v_add_f32_dpp v56, v56, v56 row_ror:8 row_mask:0xf bank_mask:0xf bound_ctrl:1
	v_add_f32_dpp v57, v57, v57 row_ror:8 row_mask:0xf bank_mask:0xf bound_ctrl:1
	v_add_f32_dpp v54, v54, v54 row_ror:8 row_mask:0xf bank_mask:0xf bound_ctrl:1
	v_add_f32_dpp v55, v55, v55 row_ror:8 row_mask:0xf bank_mask:0xf bound_ctrl:1
	v_add_f32_dpp v52, v52, v52 row_ror:8 row_mask:0xf bank_mask:0xf bound_ctrl:1
	v_add_f32_dpp v53, v53, v53 row_ror:8 row_mask:0xf bank_mask:0xf bound_ctrl:1
	v_add_f32_dpp v50, v50, v50 row_ror:8 row_mask:0xf bank_mask:0xf bound_ctrl:1
	v_add_f32_dpp v51, v51, v51 row_ror:8 row_mask:0xf bank_mask:0xf bound_ctrl:1
	v_add_f32_dpp v48, v48, v48 row_ror:8 row_mask:0xf bank_mask:0xf bound_ctrl:1
	v_add_f32_dpp v49, v49, v49 row_ror:8 row_mask:0xf bank_mask:0xf bound_ctrl:1
	v_add_f32_dpp v46, v46, v46 row_ror:8 row_mask:0xf bank_mask:0xf bound_ctrl:1
	v_add_f32_dpp v47, v47, v47 row_ror:8 row_mask:0xf bank_mask:0xf bound_ctrl:1
	v_add_f32_dpp v44, v44, v44 row_ror:8 row_mask:0xf bank_mask:0xf bound_ctrl:1
	v_add_f32_dpp v45, v45, v45 row_ror:8 row_mask:0xf bank_mask:0xf bound_ctrl:1
	v_add_f32_dpp v42, v42, v42 row_ror:8 row_mask:0xf bank_mask:0xf bound_ctrl:1
	v_add_f32_dpp v43, v43, v43 row_ror:8 row_mask:0xf bank_mask:0xf bound_ctrl:1
	v_add_f32_dpp v40, v40, v40 row_ror:8 row_mask:0xf bank_mask:0xf bound_ctrl:1
	v_add_f32_dpp v41, v41, v41 row_ror:8 row_mask:0xf bank_mask:0xf bound_ctrl:1
	v_add_f32_dpp v38, v38, v38 row_ror:8 row_mask:0xf bank_mask:0xf bound_ctrl:1
	v_add_f32_dpp v39, v39, v39 row_ror:8 row_mask:0xf bank_mask:0xf bound_ctrl:1
	v_add_f32_dpp v74, v74, v74 row_ror:8 row_mask:0xf bank_mask:0xf bound_ctrl:1
	v_add_f32_dpp v75, v75, v75 row_ror:8 row_mask:0xf bank_mask:0xf bound_ctrl:1
	v_permlane16_swap_b32_e32 v82, v50
	v_permlane16_swap_b32_e32 v83, v51
	v_permlane16_swap_b32_e32 v80, v48
	v_permlane16_swap_b32_e32 v81, v49
	v_permlane16_swap_b32_e32 v78, v46
	v_permlane16_swap_b32_e32 v79, v47
	v_permlane16_swap_b32_e32 v76, v44
	v_permlane16_swap_b32_e32 v77, v45
	v_permlane16_swap_b32_e32 v60, v42
	v_permlane16_swap_b32_e32 v61, v43
	v_permlane16_swap_b32_e32 v56, v40
	v_permlane16_swap_b32_e32 v57, v41
	v_permlane16_swap_b32_e32 v54, v38
	v_permlane16_swap_b32_e32 v55, v39
	v_permlane16_swap_b32_e32 v52, v74
	v_permlane16_swap_b32_e32 v53, v75
	v_add_f32_e32 v82, v82, v50
	v_add_f32_e32 v83, v83, v51
	v_add_f32_e32 v80, v80, v48
	v_add_f32_e32 v81, v81, v49
	v_add_f32_e32 v78, v78, v46
	v_add_f32_e32 v79, v79, v47
	v_add_f32_e32 v76, v76, v44
	v_add_f32_e32 v77, v77, v45
	v_add_f32_e32 v60, v60, v42
	v_add_f32_e32 v61, v61, v43
	v_add_f32_e32 v56, v56, v40
	v_add_f32_e32 v57, v57, v41
	v_add_f32_e32 v54, v54, v38
	v_add_f32_e32 v55, v55, v39
	v_add_f32_e32 v52, v52, v74
	v_add_f32_e32 v53, v53, v75
	v_permlane32_swap_b32_e32 v82, v60
	v_permlane32_swap_b32_e32 v83, v61
	v_permlane32_swap_b32_e32 v80, v56
	v_permlane32_swap_b32_e32 v81, v57
	v_permlane32_swap_b32_e32 v78, v54
	v_permlane32_swap_b32_e32 v79, v55
	v_permlane32_swap_b32_e32 v76, v52
	v_permlane32_swap_b32_e32 v77, v53
	v_mbcnt_lo_u32_b32 v10, -1, 0
	v_mbcnt_hi_u32_b32 v10, -1, v10
	v_and_b32_e32 v11, 7, v10
	v_lshlrev_b32_e32 v11, 4, v11
	v_bfe_u32 v12, v10, 4, 1
	v_lshl_add_u32 v11, v12, 9, v11
	v_bfe_u32 v12, v10, 5, 1
	v_lshl_add_u32 v11, v12, 8, v11
	v_add_f32_e32 v2, v82, v60
	v_add_f32_e32 v3, v83, v61
	v_add_f32_e32 v4, v80, v56
	v_add_f32_e32 v5, v81, v57
	v_add_f32_e32 v6, v78, v54
	v_add_f32_e32 v7, v79, v55
	v_add_f32_e32 v8, v76, v52
	v_add_f32_e32 v9, v77, v53
	v_readfirstlane_b32 s8, v63
	s_nop 1
	v_add_u32_e32 v11, s8, v11
	ds_write_b128 v11, v[2:5]
	ds_write_b128 v11, v[6:9] offset:128
	s_waitcnt lgkmcnt(0)
	s_barrier
	s_and_saveexec_b64 s[8:9], s[6:7]
	s_cbranch_execz .LBB0_2349
	ds_read2st64_b32 v[2:3], v99 offset1:4
	ds_read2st64_b32 v[4:5], v99 offset0:8 offset1:12
	ds_read2st64_b32 v[6:7], v99 offset0:16 offset1:20
	ds_read2st64_b32 v[8:9], v99 offset0:24 offset1:28
	s_waitcnt lgkmcnt(3)
	v_add_f32_e32 v2, 0, v2
	v_add_f32_e32 v2, v2, v3
	s_waitcnt lgkmcnt(2)
	v_add_f32_e32 v2, v2, v4
	v_add_f32_e32 v2, v2, v5
	s_waitcnt lgkmcnt(1)
	v_add_f32_e32 v2, v2, v6
	v_add_f32_e32 v2, v2, v7
	s_waitcnt lgkmcnt(0)
	v_add_f32_e32 v2, v2, v8
	v_add_f32_e32 v2, v2, v9
	v_mul_f32_e32 v3, 0xbfb8aa3b, v2
	v_fma_f32 v4, v2, s34, -v3
	v_rndne_f32_e32 v5, v3
	v_fmac_f32_e32 v4, 0xb2a5705f, v2
	v_sub_f32_e32 v3, v3, v5
	v_add_f32_e32 v3, v3, v4
	v_cvt_i32_f32_e32 v4, v5
	v_exp_f32_e32 v3, v3
	v_cmp_nlt_f32_e32 vcc, s35, v2
	v_ldexp_f32 v3, v3, v4
	s_nop 0
	v_cndmask_b32_e32 v3, 0, v3, vcc
	v_cmp_ngt_f32_e32 vcc, s36, v2
	s_nop 1
	v_cndmask_b32_e32 v2, v109, v3, vcc
	v_add_f32_e32 v2, 1.0, v2
	v_div_scale_f32 v3, s[26:27], v2, v2, 1.0
	v_rcp_f32_e32 v4, v3
	s_nop 0
	v_fma_f32 v5, -v3, v4, 1.0
	v_fmac_f32_e32 v4, v5, v4
	v_div_scale_f32 v5, vcc, 1.0, v2, 1.0
	v_mul_f32_e32 v6, v5, v4
	v_fma_f32 v7, -v3, v6, v5
	v_fmac_f32_e32 v6, v7, v4
	v_fma_f32 v3, -v3, v6, v5
	v_div_fmas_f32 v3, v3, v4, v6
	v_div_fixup_f32 v2, v3, v2, 1.0
	v_lshl_add_u32 v3, s13, 10, v100
	ds_write_b32 v3, v2
	s_branch .LBB0_2349
